# speedup vs baseline: 1.0148x; 1.0148x over previous
_Z10enc_kernelPKfS0_PK15HIP_vector_typeIjLj4EES4_S4_S0_S0_S0_Pf:
	s_load_dwordx4 s[12:15], s[0:1], 0x0
	s_load_dwordx2 s[16:17], s[0:1], 0x10
	s_load_dwordx8 s[4:11], s[0:1], 0x28
	v_lshrrev_b32_e32 v56, 6, v0
	s_lshl_b32 s2, s2, 6
	v_lshl_or_b32 v47, v56, 4, s2
	v_and_b32_e32 v57, 15, v0
	v_or_b32_e32 v2, v47, v57
	v_ashrrev_i32_e32 v3, 31, v2
	s_waitcnt lgkmcnt(0)
	v_lshl_add_u64 v[4:5], v[2:3], 2, s[14:15]
	global_load_dword v46, v[4:5], off
	v_mov_b32_e32 v45, 0
	v_lshlrev_b64 v[2:3], 9, v[2:3]
	v_lshlrev_b32_e32 v44, 4, v0
	v_lshl_add_u64 v[2:3], s[12:13], 0, v[2:3]
	v_and_b32_e32 v48, 48, v0
	v_mov_b32_e32 v49, v45
	v_lshl_add_u64 v[42:43], v[2:3], 0, v[48:49]
	global_load_dwordx4 v[98:101], v[42:43], off
	global_load_dwordx4 v[102:105], v[42:43], off offset:64
	global_load_dwordx4 v[106:109], v[42:43], off offset:128
	global_load_dwordx4 v[110:113], v[42:43], off offset:192
	global_load_dwordx4 v[10:13], v[42:43], off offset:256
	global_load_dwordx4 v[14:17], v[42:43], off offset:320
	s_nop 0
	global_load_dwordx4 v[2:5], v[42:43], off offset:384
	global_load_dwordx4 v[6:9], v[42:43], off offset:448
	v_and_b32_e32 v119, 48, v0
	global_load_dwordx4 v[120:123], v119, s[4:5]
	global_load_dwordx4 v[124:127], v119, s[4:5] offset:64
	global_load_dwordx4 v[128:131], v119, s[4:5] offset:128
	global_load_dwordx4 v[132:135], v119, s[4:5] offset:192
	global_load_dwordx4 v[136:139], v119, s[4:5] offset:256
	global_load_dwordx4 v[140:143], v119, s[4:5] offset:320
	global_load_dwordx4 v[144:147], v119, s[4:5] offset:384
	global_load_dwordx4 v[148:151], v119, s[4:5] offset:448
	global_load_dwordx4 a[0:3], v119, s[6:7]
	global_load_dwordx4 a[56:59], v119, s[6:7] offset:64
	global_load_dwordx4 a[4:7], v119, s[6:7] offset:128
	global_load_dwordx4 v[164:167], v119, s[6:7] offset:192
	global_load_dwordx4 a[32:35], v119, s[6:7] offset:256
	global_load_dwordx4 a[40:43], v119, s[6:7] offset:320
	global_load_dwordx4 a[8:11], v119, s[8:9]
	global_load_dwordx4 v[180:183], v119, s[8:9] offset:64
	global_load_dwordx4 a[12:15], v119, s[8:9] offset:128
	global_load_dwordx4 v[188:191], v119, s[8:9] offset:192
	v_lshl_add_u64 v[114:115], s[16:17], 0, v[44:45]
	s_movk_i32 s0, 0x2000
	v_add_co_u32_e32 v116, vcc, s0, v114
	s_movk_i32 s0, 0x4000
	s_nop 0
	v_addc_co_u32_e32 v117, vcc, 0, v115, vcc
	v_add_co_u32_e32 v54, vcc, s0, v114
	s_movk_i32 s0, 0x6000
	s_nop 0
	v_addc_co_u32_e32 v55, vcc, 0, v115, vcc
	global_load_dwordx4 v[18:21], v44, s[16:17]
	global_load_dwordx4 v[22:25], v[116:117], off offset:-4096
	global_load_dwordx4 v[26:29], v[116:117], off
	global_load_dwordx4 v[30:33], v[54:55], off offset:-4096
	v_add_co_u32_e32 v116, vcc, s0, v114
	s_mov_b32 s0, 0x8000
	s_nop 0
	v_addc_co_u32_e32 v117, vcc, 0, v115, vcc
	global_load_dwordx4 v[34:37], v[54:55], off
	global_load_dwordx4 v[38:41], v[116:117], off offset:-4096
	v_add_co_u32_e32 v54, vcc, s0, v114
	s_mov_b32 s0, 0xa000
	s_nop 0
	v_addc_co_u32_e32 v55, vcc, 0, v115, vcc
	global_load_dwordx4 v[50:53], v[116:117], off
	global_load_dwordx4 v[58:61], v[54:55], off offset:-4096
	v_add_co_u32_e32 v116, vcc, s0, v114
	s_mov_b32 s0, 0xc000
	s_nop 0
	v_addc_co_u32_e32 v117, vcc, 0, v115, vcc
	global_load_dwordx4 v[62:65], v[54:55], off
	global_load_dwordx4 v[66:69], v[116:117], off offset:-4096
	v_add_co_u32_e32 v54, vcc, s0, v114
	s_mov_b32 s0, 0xe000
	s_nop 0
	v_addc_co_u32_e32 v55, vcc, 0, v115, vcc
	global_load_dwordx4 v[70:73], v[116:117], off
	global_load_dwordx4 v[74:77], v[54:55], off offset:-4096
	v_add_co_u32_e32 v116, vcc, s0, v114
	s_mov_b32 s0, 0x10000
	s_nop 0
	v_addc_co_u32_e32 v117, vcc, 0, v115, vcc
	v_add_co_u32_e32 v114, vcc, s0, v114
	global_load_dwordx4 v[78:81], v[54:55], off
	global_load_dwordx4 v[82:85], v[116:117], off offset:-4096
	v_addc_co_u32_e32 v115, vcc, 0, v115, vcc
	global_load_dwordx4 v[86:89], v[116:117], off
	global_load_dwordx4 v[90:93], v[114:115], off offset:-4096
	global_load_dwordx4 v[94:97], v[114:115], off
	v_or_b32_e32 v1, 0x10000, v44
	v_and_b32_e32 v49, 63, v0
	s_movk_i32 s0, 0x1040
	s_movk_i32 s2, 0x104
	v_cmp_gt_u32_e32 vcc, 16, v49
	s_waitcnt vmcnt(16)
	ds_write_b128 v44, v[18:21]
	s_waitcnt vmcnt(15)
	ds_write_b128 v44, v[22:25] offset:4096
	s_waitcnt vmcnt(14)
	ds_write_b128 v44, v[26:29] offset:8192
	s_waitcnt vmcnt(13)
	ds_write_b128 v44, v[30:33] offset:12288
	s_waitcnt vmcnt(12)
	ds_write_b128 v44, v[34:37] offset:16384
	s_waitcnt vmcnt(11)
	ds_write_b128 v44, v[38:41] offset:20480
	s_waitcnt vmcnt(10)
	ds_write_b128 v44, v[50:53] offset:24576
	s_waitcnt vmcnt(9)
	ds_write_b128 v44, v[58:61] offset:28672
	s_waitcnt vmcnt(8)
	ds_write_b128 v44, v[62:65] offset:32768
	s_waitcnt vmcnt(7)
	ds_write_b128 v44, v[66:69] offset:36864
	s_waitcnt vmcnt(6)
	ds_write_b128 v44, v[70:73] offset:40960
	s_waitcnt vmcnt(5)
	ds_write_b128 v44, v[74:77] offset:45056
	s_waitcnt vmcnt(4)
	ds_write_b128 v44, v[78:81] offset:49152
	s_waitcnt vmcnt(3)
	ds_write_b128 v44, v[82:85] offset:53248
	s_waitcnt vmcnt(2)
	ds_write_b128 v44, v[86:89] offset:57344
	s_waitcnt vmcnt(1)
	ds_write_b128 v44, v[90:93] offset:61440
	s_waitcnt vmcnt(0)
	ds_write_b128 v1, v[94:97]
	s_waitcnt lgkmcnt(0)
	s_barrier
	s_waitcnt vmcnt(0)
	v_pk_fma_f32 v[18:19], v[98:99], -2.0, v[46:47] op_sel_hi:[1,0,0]
	v_pk_fma_f32 v[20:21], v[100:101], -2.0, v[46:47] op_sel_hi:[1,0,0]
	v_pk_fma_f32 v[22:23], v[102:103], -2.0, v[46:47] op_sel_hi:[1,0,0]
	v_pk_fma_f32 v[36:37], v[104:105], -2.0, v[46:47] op_sel_hi:[1,0,0]
	v_pk_fma_f32 v[38:39], v[106:107], -2.0, v[46:47] op_sel_hi:[1,0,0]
	v_cvt_pk_bf16_f32 v18, v18, v19
	v_cvt_pk_bf16_f32 v19, v20, v21
	v_cvt_pk_bf16_f32 v20, v22, v23
	v_cvt_pk_bf16_f32 v21, v36, v37
	v_cvt_pk_bf16_f32 v22, v38, v39
	v_lshlrev_b32_e32 v44, 4, v49
	ds_read_b128 v[58:61], v44
	ds_read_b128 v[62:65], v44 offset:1024
	ds_read_b128 v[66:69], v44 offset:4096
	ds_read_b128 v[70:73], v44 offset:5120
	ds_read_b128 v[74:77], v44 offset:8192
	ds_read_b128 v[78:81], v44 offset:9216
	ds_read_b128 v[82:85], v44 offset:12288
	ds_read_b128 v[86:89], v44 offset:13312
	v_pk_fma_f32 v[50:51], v[108:109], -2.0, v[46:47] op_sel_hi:[1,0,0]
	v_pk_fma_f32 v[52:53], v[110:111], -2.0, v[46:47] op_sel_hi:[1,0,0]
	v_pk_fma_f32 v[54:55], v[112:113], -2.0, v[46:47] op_sel_hi:[1,0,0]
	v_cvt_pk_bf16_f32 v23, v50, v51
	v_pk_fma_f32 v[0:1], v[10:11], -2.0, v[46:47] op_sel_hi:[1,0,0]
	v_pk_fma_f32 v[12:13], v[12:13], -2.0, v[46:47] op_sel_hi:[1,0,0]
	v_cvt_pk_bf16_f32 v10, v0, v1
	v_cvt_pk_bf16_f32 v11, v12, v13
	v_pk_fma_f32 v[8:9], v[8:9], -2.0, v[46:47] op_sel_hi:[1,0,0]
	v_pk_mul_f32 v[24:25], v[46:47], v[120:121] op_sel_hi:[0,1]
	v_pk_mul_f32 v[26:27], v[46:47], v[122:123] op_sel_hi:[0,1]
	v_accvgpr_write_b32 a16, v24
	v_accvgpr_write_b32 a17, v25
	v_accvgpr_write_b32 a18, v26
	v_accvgpr_write_b32 a19, v27
	v_pk_mul_f32 v[24:25], v[46:47], v[124:125] op_sel_hi:[0,1]
	v_pk_mul_f32 v[26:27], v[46:47], v[126:127] op_sel_hi:[0,1]
	v_accvgpr_write_b32 a20, v24
	v_accvgpr_write_b32 a21, v25
	v_accvgpr_write_b32 a22, v26
	v_accvgpr_write_b32 a23, v27
	v_pk_mul_f32 v[24:25], v[46:47], v[128:129] op_sel_hi:[0,1]
	v_pk_mul_f32 v[26:27], v[46:47], v[130:131] op_sel_hi:[0,1]
	v_accvgpr_write_b32 a24, v24
	v_accvgpr_write_b32 a25, v25
	v_accvgpr_write_b32 a26, v26
	v_accvgpr_write_b32 a27, v27
	v_pk_mul_f32 v[26:27], v[46:47], v[134:135] op_sel_hi:[0,1]
	v_pk_mul_f32 v[24:25], v[46:47], v[132:133] op_sel_hi:[0,1]
	v_accvgpr_write_b32 a31, v27
	v_accvgpr_write_b32 a30, v26
	v_accvgpr_write_b32 a29, v25
	v_accvgpr_write_b32 a28, v24
	v_pk_fma_f32 v[26:27], v[14:15], -2.0, v[46:47] op_sel_hi:[1,0,0]
	v_pk_fma_f32 v[28:29], v[16:17], -2.0, v[46:47] op_sel_hi:[1,0,0]
	ds_read_b128 v[14:17], v44 offset:2048
	s_waitcnt lgkmcnt(8)
	v_mfma_f32_16x16x32_bf16 a[16:19], v[58:61], v[18:21], a[16:19]
	v_cvt_pk_bf16_f32 v24, v52, v53
	v_cvt_pk_bf16_f32 v25, v54, v55
	v_cvt_pk_bf16_f32 v12, v26, v27
	s_waitcnt lgkmcnt(2)
	v_mfma_f32_16x16x32_bf16 a[28:31], v[82:85], v[18:21], a[28:31]
	v_cvt_pk_bf16_f32 v13, v28, v29
	ds_read_b128 v[26:29], v44 offset:6144
	ds_read_b128 v[40:43], v44 offset:3072
	ds_read_b128 v[50:53], v44 offset:10240
	v_mfma_f32_16x16x32_bf16 a[16:19], v[62:65], v[22:25], a[16:19]
	v_fma_f32 v34, v2, -2.0, v46
	v_fma_f32 v35, v3, -2.0, v46
	v_pk_fma_f32 v[54:55], v[6:7], -2.0, v[46:47] op_sel_hi:[1,0,0]
	v_pk_mul_f32 v[32:33], v[46:47], v[142:143] op_sel_hi:[0,1]
	s_waitcnt lgkmcnt(3)
	v_mfma_f32_16x16x32_bf16 a[16:19], v[14:17], v[10:13], a[16:19]
	ds_read_b128 v[0:3], v44 offset:7168
	ds_read_b128 v[14:17], v44 offset:14336
	v_pk_mul_f32 v[30:31], v[46:47], v[140:141] op_sel_hi:[0,1]
	v_accvgpr_write_b32 a47, v33
	v_mfma_f32_16x16x32_bf16 a[28:31], v[86:89], v[22:25], a[28:31]
	v_accvgpr_write_b32 a46, v32
	v_accvgpr_write_b32 a45, v31
	v_accvgpr_write_b32 a44, v30
	s_waitcnt lgkmcnt(0)
	v_mfma_f32_16x16x32_bf16 a[28:31], v[14:17], v[10:13], a[28:31]
	s_nop 1
	ds_read_b128 v[30:33], v44 offset:23552
	v_mfma_f32_16x16x32_bf16 a[20:23], v[66:69], v[18:21], a[20:23]
	v_mfma_f32_16x16x32_bf16 a[20:23], v[70:73], v[22:25], a[20:23]
	v_mfma_f32_16x16x32_bf16 a[20:23], v[26:29], v[10:13], a[20:23]
	v_fma_f32 v28, v4, -2.0, v46
	v_fma_f32 v29, v5, -2.0, v46
	v_cvt_pk_bf16_f32 v26, v34, v35
	v_cvt_pk_bf16_f32 v27, v28, v29
	v_cvt_pk_bf16_f32 v28, v54, v55
	v_cvt_pk_bf16_f32 v29, v8, v9
	v_mfma_f32_16x16x32_bf16 a[24:27], v[74:77], v[18:21], a[24:27]
	ds_read_b128 v[4:7], v44 offset:11264
	v_pk_mul_f32 v[34:35], v[46:47], v[136:137] op_sel_hi:[0,1]
	v_pk_mul_f32 v[36:37], v[46:47], v[138:139] op_sel_hi:[0,1]
	v_mfma_f32_16x16x32_bf16 a[20:23], v[0:3], v[26:29], a[20:23]
	s_nop 1
	v_accvgpr_write_b32 a39, v37
	v_accvgpr_write_b32 a38, v36
	v_mfma_f32_16x16x32_bf16 a[24:27], v[78:81], v[22:25], a[24:27]
	v_accvgpr_write_b32 a37, v35
	v_accvgpr_write_b32 a36, v34
	ds_read_b128 v[34:37], v44 offset:19456
	v_mfma_f32_16x16x32_bf16 a[24:27], v[50:53], v[10:13], a[24:27]
	ds_read_b128 v[50:53], v44 offset:15360
	v_pk_mul_f32 v[16:17], v[46:47], v[146:147] op_sel_hi:[0,1]
	s_waitcnt lgkmcnt(2)
	v_mfma_f32_16x16x32_bf16 a[24:27], v[4:7], v[26:29], a[24:27]
	ds_read_b128 v[4:7], v44 offset:16384
	v_pk_mul_f32 v[14:15], v[46:47], v[144:145] op_sel_hi:[0,1]
	v_accvgpr_write_b32 a51, v17
	v_mfma_f32_16x16x32_bf16 a[16:19], v[40:43], v[26:29], a[16:19]
	ds_read_b128 v[40:43], v44 offset:17408
	v_accvgpr_write_b32 a50, v16
	v_accvgpr_write_b32 a49, v15
	s_waitcnt lgkmcnt(1)
	v_mfma_f32_16x16x32_bf16 a[36:39], v[4:7], v[18:21], a[36:39]
	ds_read_b128 v[4:7], v44 offset:18432
	v_accvgpr_write_b32 a48, v14
	ds_read_b128 v[14:17], v44 offset:27648
	s_waitcnt lgkmcnt(2)
	v_mfma_f32_16x16x32_bf16 a[36:39], v[40:43], v[22:25], a[36:39]
	v_pk_mul_f32 v[2:3], v[46:47], v[150:151] op_sel_hi:[0,1]
	s_waitcnt lgkmcnt(1)
	v_mfma_f32_16x16x32_bf16 a[36:39], v[4:7], v[10:13], a[36:39]
	ds_read_b128 v[4:7], v44 offset:20480
	v_pk_mul_f32 v[0:1], v[46:47], v[148:149] op_sel_hi:[0,1]
	v_accvgpr_write_b32 a55, v3
	v_mfma_f32_16x16x32_bf16 a[36:39], v[34:37], v[26:29], a[36:39]
	ds_read_b128 v[34:37], v44 offset:21504
	v_accvgpr_write_b32 a54, v2
	v_accvgpr_write_b32 a53, v1
	s_waitcnt lgkmcnt(1)
	v_mfma_f32_16x16x32_bf16 a[44:47], v[4:7], v[18:21], a[44:47]
	ds_read_b128 v[4:7], v44 offset:22528
	v_accvgpr_write_b32 a52, v0
	ds_read_b128 v[0:3], v44 offset:30720
	s_waitcnt lgkmcnt(2)
	v_mfma_f32_16x16x32_bf16 a[44:47], v[34:37], v[22:25], a[44:47]
	v_accvgpr_read_b32 v9, a36
	s_waitcnt lgkmcnt(1)
	v_mfma_f32_16x16x32_bf16 a[44:47], v[4:7], v[10:13], a[44:47]
	ds_read_b128 v[4:7], v44 offset:24576
	v_mfma_f32_16x16x32_bf16 a[44:47], v[30:33], v[26:29], a[44:47]
	ds_read_b128 v[30:33], v44 offset:25600
	s_waitcnt lgkmcnt(1)
	v_mfma_f32_16x16x32_bf16 a[48:51], v[4:7], v[18:21], a[48:51]
	ds_read_b128 v[4:7], v44 offset:26624
	s_waitcnt lgkmcnt(1)
	v_mfma_f32_16x16x32_bf16 a[48:51], v[30:33], v[22:25], a[48:51]
	s_waitcnt lgkmcnt(0)
	v_mfma_f32_16x16x32_bf16 a[48:51], v[4:7], v[10:13], a[48:51]
	ds_read_b128 v[4:7], v44 offset:28672
	v_mfma_f32_16x16x32_bf16 a[48:51], v[14:17], v[26:29], a[48:51]
	ds_read_b128 v[14:17], v44 offset:29696
	s_waitcnt lgkmcnt(1)
	v_mfma_f32_16x16x32_bf16 a[52:55], v[4:7], v[18:21], a[52:55]
	ds_read_b128 v[4:7], v44 offset:31744
	s_nop 3
	v_accvgpr_read_b32 v20, a49
	s_waitcnt lgkmcnt(1)
	v_mfma_f32_16x16x32_bf16 a[52:55], v[14:17], v[22:25], a[52:55]
	v_accvgpr_read_b32 v16, a46
	v_accvgpr_read_b32 v21, a48
	v_cvt_pk_bf16_f32 v20, v21, v20
	v_mfma_f32_16x16x32_bf16 a[52:55], v[0:3], v[10:13], a[52:55]
	v_accvgpr_read_b32 v0, a17
	v_accvgpr_read_b32 v1, a16
	v_cvt_pk_bf16_f32 v0, v1, v0
	v_accvgpr_read_b32 v1, a19
	v_accvgpr_read_b32 v2, a18
	v_mfma_f32_16x16x32_bf16 a[28:31], v[50:53], v[26:29], a[28:31]
	v_cvt_pk_bf16_f32 v1, v2, v1
	v_accvgpr_read_b32 v2, a21
	v_accvgpr_read_b32 v3, a20
	s_waitcnt lgkmcnt(0)
	v_mfma_f32_16x16x32_bf16 a[52:55], v[4:7], v[26:29], a[52:55]
	v_cvt_pk_bf16_f32 v2, v3, v2
	v_accvgpr_read_b32 v3, a23
	v_accvgpr_read_b32 v4, a22
	v_cvt_pk_bf16_f32 v3, v4, v3
	v_accvgpr_read_b32 v4, a25
	v_accvgpr_read_b32 v5, a24
	v_cvt_pk_bf16_f32 v4, v5, v4
	v_accvgpr_read_b32 v5, a27
	v_accvgpr_read_b32 v6, a26
	v_cvt_pk_bf16_f32 v5, v6, v5
	v_accvgpr_read_b32 v6, a29
	v_accvgpr_read_b32 v7, a28
	v_cvt_pk_bf16_f32 v6, v7, v6
	v_accvgpr_read_b32 v7, a31
	v_accvgpr_read_b32 v8, a30
	v_cvt_pk_bf16_f32 v7, v8, v7
	v_accvgpr_read_b32 v8, a37
	ds_read_b128 v[12:15], v44 offset:32768
	v_cvt_pk_bf16_f32 v8, v9, v8
	v_accvgpr_read_b32 v9, a39
	v_accvgpr_read_b32 v10, a38
	v_cvt_pk_bf16_f32 v9, v10, v9
	v_accvgpr_read_b32 v10, a45
	v_accvgpr_read_b32 v11, a44
	v_cvt_pk_bf16_f32 v10, v11, v10
	v_accvgpr_read_b32 v11, a47
	v_cvt_pk_bf16_f32 v11, v16, v11
	ds_read_b128 v[16:19], v44 offset:33792
	ds_read_b128 v[24:27], v44 offset:34816
	s_waitcnt lgkmcnt(2)
	v_mfma_f32_16x16x32_bf16 a[0:3], v[12:15], v[0:3], a[0:3]
	v_accvgpr_read_b32 v21, a51
	v_accvgpr_read_b32 v12, a50
	v_cvt_pk_bf16_f32 v21, v12, v21
	ds_read_b128 v[12:15], v44 offset:35840
	s_waitcnt lgkmcnt(2)
	v_mfma_f32_16x16x32_bf16 a[0:3], v[16:19], v[4:7], a[0:3]
	v_accvgpr_read_b32 v16, a53
	v_accvgpr_read_b32 v17, a52
	v_cvt_pk_bf16_f32 v22, v17, v16
	s_waitcnt lgkmcnt(1)
	v_mfma_f32_16x16x32_bf16 a[0:3], v[24:27], v[8:11], a[0:3]
	v_accvgpr_read_b32 v16, a55
	v_accvgpr_read_b32 v17, a54
	v_accvgpr_write_b32 a16, v164
	v_accvgpr_write_b32 a17, v165
	v_accvgpr_write_b32 a18, v166
	v_accvgpr_write_b32 a19, v167
	v_cvt_pk_bf16_f32 v23, v17, v16
	v_accvgpr_write_b32 a20, v180
	v_accvgpr_write_b32 a21, v181
	v_accvgpr_write_b32 a22, v182
	v_accvgpr_write_b32 a23, v183
	s_waitcnt lgkmcnt(0)
	v_mfma_f32_16x16x32_bf16 a[0:3], v[12:15], v[20:23], a[0:3]
	s_nop 7
	v_accvgpr_read_b32 v12, a0
	v_mul_f32_e32 v12, 0x4038aa3b, v12
	v_exp_f32_e32 v16, v12
	v_accvgpr_read_b32 v12, a1
	v_mul_f32_e32 v12, 0x4038aa3b, v12
	v_exp_f32_e32 v17, v12
	ds_read_b128 v[12:15], v44 offset:36864
	v_add_f32_e32 v16, 1.0, v16
	v_rcp_f32_e32 v28, v16
	v_add_f32_e32 v24, 1.0, v17
	ds_read_b128 v[16:19], v44 offset:37888
	v_rcp_f32_e32 v29, v24
	ds_read_b128 v[24:27], v44 offset:38912
	s_waitcnt lgkmcnt(2)
	v_mfma_f32_16x16x32_bf16 a[24:27], v[12:15], v[0:3], a[56:59]
	v_accvgpr_read_b32 v30, a2
	v_mul_f32_e32 v12, 0x4038aa3b, v30
	v_exp_f32_e32 v30, v12
	ds_read_b128 v[12:15], v44 offset:39936
	s_waitcnt lgkmcnt(2)
	v_mfma_f32_16x16x32_bf16 a[24:27], v[16:19], v[4:7], a[24:27]
	v_accvgpr_read_b32 v16, a3
	v_mul_f32_e32 v16, 0x4038aa3b, v16
	v_exp_f32_e32 v17, v16
	s_waitcnt lgkmcnt(1)
	v_mfma_f32_16x16x32_bf16 a[0:3], v[24:27], v[8:11], a[24:27]
	v_add_f32_e32 v16, 1.0, v30
	v_rcp_f32_e32 v16, v16
	v_add_f32_e32 v17, 1.0, v17
	s_waitcnt lgkmcnt(0)
	v_mfma_f32_16x16x32_bf16 a[0:3], v[12:15], v[20:23], a[0:3]
	v_rcp_f32_e32 v17, v17
	v_pk_fma_f32 v[28:29], v[28:29], -2.0, 1.0 op_sel_hi:[1,0,0]
	v_pk_fma_f32 v[30:31], v[16:17], -2.0, 1.0 op_sel_hi:[1,0,0]
	s_nop 4
	v_accvgpr_read_b32 v12, a0
	v_mul_f32_e32 v12, 0x4038aa3b, v12
	v_accvgpr_read_b32 v13, a1
	v_exp_f32_e32 v12, v12
	v_mul_f32_e32 v13, 0x4038aa3b, v13
	v_exp_f32_e32 v13, v13
	v_accvgpr_read_b32 v35, a3
	v_add_f32_e32 v12, 1.0, v12
	v_rcp_f32_e32 v24, v12
	v_add_f32_e32 v18, 1.0, v13
	ds_read_b128 v[12:15], v44 offset:40960
	v_rcp_f32_e32 v25, v18
	ds_read_b128 v[16:19], v44 offset:41984
	s_waitcnt lgkmcnt(1)
	v_mfma_f32_16x16x32_bf16 a[4:7], v[12:15], v[0:3], a[4:7]
	v_fma_f32 v32, v24, -2.0, 1.0
	v_fma_f32 v33, v25, -2.0, 1.0
	v_accvgpr_read_b32 v24, a2
	v_mul_f32_e32 v34, 0x4038aa3b, v24
	ds_read_b128 v[24:27], v44 offset:43008
	ds_read_b128 v[12:15], v44 offset:44032
	s_waitcnt lgkmcnt(2)
	v_mfma_f32_16x16x32_bf16 a[0:3], v[16:19], v[4:7], a[4:7]
	v_mul_f32_e32 v16, 0x4038aa3b, v35
	v_exp_f32_e32 v16, v16
	v_exp_f32_e32 v34, v34
	s_waitcnt lgkmcnt(1)
	v_mfma_f32_16x16x32_bf16 a[0:3], v[24:27], v[8:11], a[0:3]
	v_add_f32_e32 v16, 1.0, v16
	v_rcp_f32_e32 v35, v16
	v_add_f32_e32 v17, 1.0, v34
	s_waitcnt lgkmcnt(0)
	v_mfma_f32_16x16x32_bf16 a[0:3], v[12:15], v[20:23], a[0:3]
	v_rcp_f32_e32 v34, v17
	v_accvgpr_write_b32 a4, v188
	v_accvgpr_write_b32 a5, v189
	v_accvgpr_write_b32 a6, v190
	v_accvgpr_write_b32 a7, v191
	v_pk_fma_f32 v[34:35], v[34:35], -2.0, 1.0 op_sel_hi:[1,0,0]
	s_nop 4
	v_accvgpr_read_b32 v12, a0
	v_mul_f32_e32 v12, 0x4038aa3b, v12
	v_exp_f32_e32 v16, v12
	v_accvgpr_read_b32 v12, a1
	v_mul_f32_e32 v12, 0x4038aa3b, v12
	v_exp_f32_e32 v17, v12
	ds_read_b128 v[12:15], v44 offset:45056
	v_add_f32_e32 v16, 1.0, v16
	v_rcp_f32_e32 v36, v16
	v_add_f32_e32 v24, 1.0, v17
	ds_read_b128 v[16:19], v44 offset:46080
	v_rcp_f32_e32 v37, v24
	ds_read_b128 v[24:27], v44 offset:47104
	s_waitcnt lgkmcnt(2)
	v_mfma_f32_16x16x32_bf16 a[16:19], v[12:15], v[0:3], a[16:19]
	v_accvgpr_read_b32 v38, a2
	v_mul_f32_e32 v12, 0x4038aa3b, v38
	v_exp_f32_e32 v38, v12
	ds_read_b128 v[12:15], v44 offset:48128
	s_waitcnt lgkmcnt(2)
	v_mfma_f32_16x16x32_bf16 a[16:19], v[16:19], v[4:7], a[16:19]
	v_accvgpr_read_b32 v17, a3
	v_mul_f32_e32 v17, 0x4038aa3b, v17
	v_exp_f32_e32 v17, v17
	s_waitcnt lgkmcnt(1)
	v_mfma_f32_16x16x32_bf16 a[16:19], v[24:27], v[8:11], a[16:19]
	v_add_f32_e32 v16, 1.0, v38
	v_rcp_f32_e32 v38, v16
	v_pk_fma_f32 v[36:37], v[36:37], -2.0, 1.0 op_sel_hi:[1,0,0]
	s_waitcnt lgkmcnt(0)
	v_mfma_f32_16x16x32_bf16 a[0:3], v[12:15], v[20:23], a[16:19]
	v_add_f32_e32 v13, 1.0, v17
	v_rcp_f32_e32 v39, v13
	s_nop 0
	v_pk_fma_f32 v[38:39], v[38:39], -2.0, 1.0 op_sel_hi:[1,0,0]
	s_nop 3
	v_accvgpr_read_b32 v12, a0
	v_mul_f32_e32 v12, 0x4038aa3b, v12
	v_exp_f32_e32 v12, v12
	v_accvgpr_read_b32 v17, a2
	v_mul_f32_e32 v17, 0x4038aa3b, v17
	v_exp_f32_e32 v24, v17
	v_add_f32_e32 v12, 1.0, v12
	v_rcp_f32_e32 v40, v12
	v_accvgpr_read_b32 v12, a1
	v_mul_f32_e32 v12, 0x4038aa3b, v12
	v_exp_f32_e32 v16, v12
	ds_read_b128 v[12:15], v44 offset:49152
	v_add_f32_e32 v42, 1.0, v24
	v_accvgpr_read_b32 v43, a3
	v_add_f32_e32 v25, 1.0, v16
	ds_read_b128 v[16:19], v44 offset:50176
	v_rcp_f32_e32 v41, v25
	ds_read_b128 v[24:27], v44 offset:51200
	s_waitcnt lgkmcnt(2)
	v_mfma_f32_16x16x32_bf16 a[0:3], v[12:15], v[0:3], a[32:35]
	v_mul_f32_e32 v12, 0x4038aa3b, v43
	v_exp_f32_e32 v43, v12
	ds_read_b128 v[12:15], v44 offset:52224
	s_waitcnt lgkmcnt(2)
	v_mfma_f32_16x16x32_bf16 a[0:3], v[16:19], v[4:7], a[0:3]
	v_rcp_f32_e32 v16, v42
	v_add_f32_e32 v17, 1.0, v43
	v_rcp_f32_e32 v17, v17
	s_waitcnt lgkmcnt(1)
	v_mfma_f32_16x16x32_bf16 a[0:3], v[24:27], v[8:11], a[0:3]
	v_fma_f32 v40, v40, -2.0, 1.0
	v_fma_f32 v41, v41, -2.0, 1.0
	v_pk_fma_f32 v[42:43], v[16:17], -2.0, 1.0 op_sel_hi:[1,0,0]
	s_waitcnt lgkmcnt(0)
	v_mfma_f32_16x16x32_bf16 a[0:3], v[12:15], v[20:23], a[0:3]
	s_nop 7
	v_accvgpr_read_b32 v12, a0
	v_mul_f32_e32 v12, 0x4038aa3b, v12
	v_exp_f32_e32 v16, v12
	v_accvgpr_read_b32 v12, a1
	v_mul_f32_e32 v17, 0x4038aa3b, v12
	ds_read_b128 v[12:15], v44 offset:53248
	v_exp_f32_e32 v24, v17
	v_add_f32_e32 v16, 1.0, v16
	v_rcp_f32_e32 v50, v16
	ds_read_b128 v[16:19], v44 offset:54272
	v_add_f32_e32 v24, 1.0, v24
	v_rcp_f32_e32 v51, v24
	ds_read_b128 v[24:27], v44 offset:55296
	s_waitcnt lgkmcnt(2)
	v_mfma_f32_16x16x32_bf16 a[16:19], v[12:15], v[0:3], a[40:43]
	v_accvgpr_read_b32 v52, a2
	v_mul_f32_e32 v0, 0x4038aa3b, v52
	v_exp_f32_e32 v12, v0
	ds_read_b128 v[0:3], v44 offset:56320
	s_waitcnt lgkmcnt(2)
	v_mfma_f32_16x16x32_bf16 a[16:19], v[16:19], v[4:7], a[16:19]
	v_accvgpr_read_b32 v4, a3
	v_mul_f32_e32 v4, 0x4038aa3b, v4
	v_exp_f32_e32 v5, v4
	s_waitcnt lgkmcnt(1)
	v_mfma_f32_16x16x32_bf16 a[0:3], v[24:27], v[8:11], a[16:19]
	v_add_f32_e32 v4, 1.0, v12
	ds_read_b128 v[10:13], v44 offset:57344
	v_add_f32_e32 v5, 1.0, v5
	s_waitcnt lgkmcnt(1)
	v_mfma_f32_16x16x32_bf16 a[0:3], v[0:3], v[20:23], a[0:3]
	v_rcp_f32_e32 v4, v4
	v_rcp_f32_e32 v5, v5
	ds_read_b128 v[18:21], v44 offset:58368
	v_pk_fma_f32 v[14:15], v[50:51], -2.0, 1.0 op_sel_hi:[1,0,0]
	v_cvt_pk_bf16_f32 v6, v36, v37
	v_pk_fma_f32 v[16:17], v[4:5], -2.0, 1.0 op_sel_hi:[1,0,0]
	v_cvt_pk_bf16_f32 v4, v32, v33
	v_cvt_pk_bf16_f32 v5, v34, v35
	v_accvgpr_read_b32 v2, a2
	v_accvgpr_read_b32 v3, a3
	v_mul_f32_e32 v2, 0x4038aa3b, v2
	v_mul_f32_e32 v3, 0x4038aa3b, v3
	v_exp_f32_e32 v2, v2
	v_exp_f32_e32 v3, v3
	v_accvgpr_read_b32 v0, a0
	v_accvgpr_read_b32 v1, a1
	v_add_f32_e32 v2, 1.0, v2
	v_add_f32_e32 v3, 1.0, v3
	v_rcp_f32_e32 v2, v2
	v_rcp_f32_e32 v3, v3
	v_mul_f32_e32 v0, 0x4038aa3b, v0
	v_mul_f32_e32 v1, 0x4038aa3b, v1
	v_exp_f32_e32 v0, v0
	v_exp_f32_e32 v1, v1
	v_pk_fma_f32 v[22:23], v[2:3], -2.0, 1.0 op_sel_hi:[1,0,0]
	v_cvt_pk_bf16_f32 v2, v28, v29
	v_cvt_pk_bf16_f32 v3, v30, v31
	v_cvt_pk_bf16_f32 v14, v14, v15
	v_cvt_pk_bf16_f32 v15, v16, v17
	v_cvt_pk_bf16_f32 v17, v22, v23
	ds_read_b128 v[22:25], v44 offset:59392
	s_waitcnt lgkmcnt(2)
	v_mfma_f32_16x16x32_bf16 a[0:3], v[10:13], v[2:5], a[8:11]
	ds_read_b128 v[10:13], v44 offset:60416
	v_add_f32_e32 v0, 1.0, v0
	v_add_f32_e32 v1, 1.0, v1
	v_rcp_f32_e32 v0, v0
	v_rcp_f32_e32 v1, v1
	v_cvt_pk_bf16_f32 v7, v38, v39
	v_cvt_pk_bf16_f32 v8, v40, v41
	v_cvt_pk_bf16_f32 v9, v42, v43
	v_pk_fma_f32 v[0:1], v[0:1], -2.0, 1.0 op_sel_hi:[1,0,0]
	s_waitcnt lgkmcnt(0)
	v_mfma_f32_16x16x32_bf16 a[8:11], v[10:13], v[2:5], a[20:23]
	v_cvt_pk_bf16_f32 v16, v0, v1
	v_mov_b32_e32 v0, 0x11000
	v_mad_u32_u24 v0, v56, s0, v0
	v_mfma_f32_16x16x32_bf16 a[0:3], v[18:21], v[6:9], a[0:3]
	ds_read_b128 v[18:21], v44 offset:61440
	v_mad_u32_u24 v1, v57, s2, v0
	v_add_u32_e32 v26, v1, v48
	v_mfma_f32_16x16x32_bf16 a[0:3], v[22:25], v[14:17], a[0:3]
	ds_read_b128 v[22:25], v44 offset:62464
	s_waitcnt lgkmcnt(1)
	v_mfma_f32_16x16x32_bf16 a[8:11], v[18:21], v[6:9], a[8:11]
	ds_read_b128 v[18:21], v44 offset:64512
	s_nop 3
	v_accvgpr_read_b32 v27, a1
	v_accvgpr_read_b32 v10, a0
	ds_write2_b32 v26, v10, v27 offset0:1 offset1:2
	v_accvgpr_read_b32 v10, a3
	v_accvgpr_read_b32 v11, a2
	ds_write2_b32 v26, v11, v10 offset0:3 offset1:4
	ds_read_b128 v[10:13], v44 offset:63488
	s_waitcnt lgkmcnt(4)
	v_mfma_f32_16x16x32_bf16 a[0:3], v[22:25], v[14:17], a[8:11]
	s_nop 7
	v_accvgpr_read_b32 v22, a1
	v_accvgpr_read_b32 v23, a0
	ds_write2_b32 v26, v23, v22 offset0:17 offset1:18
	v_or_b32_e32 v22, 0x10000, v44
	ds_read_b128 v[22:25], v22
	s_waitcnt lgkmcnt(2)
	v_mfma_f32_16x16x32_bf16 a[8:11], v[10:13], v[2:5], a[12:15]
	v_or_b32_e32 v10, 0x10400, v44
	ds_read_b128 v[10:13], v10
	v_accvgpr_read_b32 v27, a3
	v_mfma_f32_16x16x32_bf16 a[8:11], v[18:21], v[6:9], a[8:11]
	v_or_b32_e32 v18, 0x10800, v44
	ds_read_b128 v[18:21], v18
	v_accvgpr_read_b32 v28, a2
	s_waitcnt lgkmcnt(2)
	v_mfma_f32_16x16x32_bf16 a[0:3], v[22:25], v[14:17], a[8:11]
	v_or_b32_e32 v22, 0x10c00, v44
	ds_read_b128 v[22:25], v22
	ds_write2_b32 v26, v28, v27 offset0:19 offset1:20
	s_waitcnt lgkmcnt(3)
	v_mfma_f32_16x16x32_bf16 a[4:7], v[10:13], v[2:5], a[4:7]
	s_waitcnt lgkmcnt(2)
	v_mfma_f32_16x16x32_bf16 a[4:7], v[18:21], v[6:9], a[4:7]
	s_nop 0
	v_accvgpr_read_b32 v2, a1
	v_accvgpr_read_b32 v3, a0
	ds_write2_b32 v26, v3, v2 offset0:33 offset1:34
	v_accvgpr_read_b32 v2, a3
	v_accvgpr_read_b32 v3, a2
	s_waitcnt lgkmcnt(2)
	v_mfma_f32_16x16x32_bf16 a[0:3], v[22:25], v[14:17], a[4:7]
	ds_write2_b32 v26, v3, v2 offset0:35 offset1:36
	s_nop 6
	v_accvgpr_read_b32 v2, a1
	v_accvgpr_read_b32 v3, a0
	ds_write2_b32 v26, v3, v2 offset0:49 offset1:50
	v_accvgpr_read_b32 v2, a3
	v_accvgpr_read_b32 v3, a2
	ds_write2_b32 v26, v3, v2 offset0:51 offset1:52
	s_and_saveexec_b64 s[0:1], vcc
	ds_write_b32 v1, v46
	s_or_b64 exec, exec, s[0:1]
	v_add_u32_e32 v2, v0, v44
	v_mov_b64_e32 v[0:1], s[10:11]
	v_mad_u64_u32 v[0:1], s[0:1], v47, s2, v[0:1]
	ds_read_b128 v[4:7], v2
	v_lshl_add_u64 v[8:9], v[0:1], 0, v[44:45]
	s_waitcnt lgkmcnt(0)
	global_store_dwordx4 v[8:9], v[4:7], off sc1
	s_nop 1
	s_mov_b64 s[0:1], 0x400
	ds_read_b128 v[4:7], v2 offset:1024
	v_lshl_add_u64 v[10:11], v[8:9], 0, s[0:1]
	s_waitcnt lgkmcnt(0)
	global_store_dwordx4 v[10:11], v[4:7], off sc1
	s_nop 1
	s_mov_b64 s[0:1], 0x800
	ds_read_b128 v[4:7], v2 offset:2048
	v_lshl_add_u64 v[10:11], v[8:9], 0, s[0:1]
	s_waitcnt lgkmcnt(0)
	global_store_dwordx4 v[10:11], v[4:7], off sc1
	s_nop 1
	s_mov_b64 s[0:1], 0xc00
	ds_read_b128 v[4:7], v2 offset:3072
	v_lshl_add_u64 v[8:9], v[8:9], 0, s[0:1]
	s_waitcnt lgkmcnt(0)
	global_store_dwordx4 v[8:9], v[4:7], off sc1
	s_nop 1
	v_or_b32_e32 v3, 0x100, v49
	v_cmp_gt_u32_e32 vcc, s2, v3
	s_and_saveexec_b64 s[0:1], vcc
	s_cbranch_execz .LBB2_4
	ds_read_b128 v[4:7], v2 offset:4096
	v_lshlrev_b32_e32 v2, 4, v3
	v_mov_b32_e32 v3, 0
	v_lshl_add_u64 v[0:1], v[0:1], 0, v[2:3]
	s_waitcnt lgkmcnt(0)
	global_store_dwordx4 v[0:1], v[4:7], off sc1
	s_nop 1
